# stream: step order rotated by an even amount per block (2*(blk&3)), keeping rows 2m,2m+1 adjacent in time; rest as v40
# baseline (speedup 1.0000x reference)
.LBB1_2:
	s_or_b64 exec, exec, s[0:1]
	s_lshr_b32 s8, s3, 6
	s_add_i32 s8, s8, s2
	s_and_b32 s8, s8, 15
	s_lshl_b32 s0, s2, 7
	v_and_b32_e32 v24, 63, v0
	s_add_i32 s9, s8, s0
	s_waitcnt lgkmcnt(0)
	s_and_b32 s1, s5, 0xffff
	s_mov_b32 s3, 0x20000
	s_brev_b32 s2, 16
	s_mov_b32 s0, s4
	v_lshlrev_b32_e32 v25, 4, v24
	s_lshl_b32 s4, s9, 12
	s_lshr_b32 s11, s9, 7
	s_and_b32 s11, s11, 3
	s_lshl_b32 s11, s11, 1
	s_add_i32 s12, s11, 0
	s_and_b32 s12, s12, 7
	s_lshl_b32 s12, s12, 16
	s_add_i32 s16, s4, s12
	s_add_i32 s12, s11, 1
	s_and_b32 s12, s12, 7
	s_lshl_b32 s12, s12, 16
	s_add_i32 s17, s4, s12
	s_add_i32 s12, s11, 2
	s_and_b32 s12, s12, 7
	s_lshl_b32 s12, s12, 16
	s_add_i32 s18, s4, s12
	s_add_i32 s12, s11, 3
	s_and_b32 s12, s12, 7
	s_lshl_b32 s12, s12, 16
	s_add_i32 s19, s4, s12
	s_add_i32 s12, s11, 4
	s_and_b32 s12, s12, 7
	s_lshl_b32 s12, s12, 16
	s_add_i32 s20, s4, s12
	s_add_i32 s12, s11, 5
	s_and_b32 s12, s12, 7
	s_lshl_b32 s12, s12, 16
	s_add_i32 s21, s4, s12
	s_add_i32 s12, s11, 6
	s_and_b32 s12, s12, 7
	s_lshl_b32 s12, s12, 16
	s_add_i32 s22, s4, s12
	s_add_i32 s12, s11, 7
	s_and_b32 s12, s12, 7
	s_lshl_b32 s12, s12, 16
	s_add_i32 s23, s4, s12
	buffer_load_dwordx4 v[26:29], v25, s[0:3], s16 offen offset:1024 nt
	buffer_load_dwordx4 v[30:33], v25, s[0:3], s16 offen nt
	buffer_load_dwordx4 v[34:37], v25, s[0:3], s16 offen offset:2048 nt
	s_barrier
	buffer_load_dwordx4 v[38:41], v25, s[0:3], s17 offen offset:1024 nt
	buffer_load_dwordx4 v[42:45], v25, s[0:3], s17 offen nt
	buffer_load_dwordx4 v[16:19], v25, s[0:3], s16 offen offset:3072 nt
	buffer_load_dwordx4 v[46:49], v25, s[0:3], s17 offen offset:2048 nt
	buffer_load_dwordx4 v[20:23], v25, s[0:3], s17 offen offset:3072 nt
	buffer_load_dwordx4 v[50:53], v25, s[0:3], s18 offen offset:1024 nt
	buffer_load_dwordx4 v[54:57], v25, s[0:3], s18 offen nt
	ds_read_b128 v[4:7], v25 offset:1024
	ds_read_b128 v[0:3], v25
	ds_read_b128 v[12:15], v25 offset:2048
	ds_read_b128 v[8:11], v25 offset:3072
	v_cmp_gt_u32_e32 vcc, 8, v24
	s_waitcnt vmcnt(9) lgkmcnt(3)
	v_pk_mul_f32 v[28:29], v[6:7], v[28:29]
	v_pk_mul_f32 v[26:27], v[4:5], v[26:27]
	s_waitcnt vmcnt(8) lgkmcnt(2)
	v_pk_fma_f32 v[32:33], v[2:3], v[32:33], v[28:29]
	v_pk_fma_f32 v[30:31], v[0:1], v[30:31], v[26:27]
	buffer_load_dwordx4 v[26:29], v25, s[0:3], s19 offen offset:1024 nt
	s_waitcnt vmcnt(8) lgkmcnt(1)
	v_pk_fma_f32 v[58:59], v[14:15], v[36:37], v[32:33]
	v_pk_fma_f32 v[60:61], v[12:13], v[34:35], v[30:31]
	buffer_load_dwordx4 v[30:33], v25, s[0:3], s19 offen nt
	s_waitcnt vmcnt(8)
	v_pk_mul_f32 v[34:35], v[6:7], v[40:41]
	v_pk_mul_f32 v[36:37], v[4:5], v[38:39]
	s_waitcnt vmcnt(7)
	v_pk_fma_f32 v[44:45], v[2:3], v[44:45], v[34:35]
	v_pk_fma_f32 v[42:43], v[0:1], v[42:43], v[36:37]
	buffer_load_dwordx4 v[34:37], v25, s[0:3], s18 offen offset:2048 nt
	s_waitcnt vmcnt(4)
	v_pk_mul_f32 v[38:39], v[6:7], v[52:53]
	v_pk_mul_f32 v[40:41], v[4:5], v[50:51]
	s_waitcnt vmcnt(3)
	v_pk_fma_f32 v[50:51], v[2:3], v[56:57], v[38:39]
	v_pk_fma_f32 v[52:53], v[0:1], v[54:55], v[40:41]
	buffer_load_dwordx4 v[38:41], v25, s[0:3], s18 offen offset:3072 nt
	v_pk_fma_f32 v[48:49], v[14:15], v[48:49], v[44:45]
	v_pk_fma_f32 v[46:47], v[12:13], v[46:47], v[42:43]
	s_waitcnt lgkmcnt(0)
	v_pk_fma_f32 v[18:19], v[10:11], v[18:19], v[58:59]
	v_pk_fma_f32 v[16:17], v[8:9], v[16:17], v[60:61]
	v_add_f32_e32 v61, v18, v19
	v_add_f32_e32 v60, v16, v17
	v_pk_fma_f32 v[16:17], v[10:11], v[22:23], v[48:49]
	v_pk_fma_f32 v[18:19], v[8:9], v[20:21], v[46:47]
	v_add_f32_e32 v16, v16, v17
	v_add_f32_e32 v18, v18, v19
	v_add_f32_e32 v60, v60, v61
	v_add_f32_e32 v16, v18, v16
	s_waitcnt vmcnt(3)
	v_pk_mul_f32 v[28:29], v[6:7], v[28:29]
	v_pk_mul_f32 v[26:27], v[4:5], v[26:27]
	v_add_f32_dpp v16, v16, v16 quad_perm:[1,0,3,2] row_mask:0xf bank_mask:0xf bound_ctrl:1
	s_waitcnt vmcnt(2)
	v_pk_fma_f32 v[54:55], v[2:3], v[32:33], v[28:29]
	v_pk_fma_f32 v[56:57], v[0:1], v[30:31], v[26:27]
	buffer_load_dwordx4 v[26:29], v25, s[0:3], s19 offen offset:2048 nt
	buffer_load_dwordx4 v[30:33], v25, s[0:3], s19 offen offset:3072 nt
	buffer_load_dwordx4 v[42:45], v25, s[0:3], s20 offen offset:1024 nt
	s_waitcnt vmcnt(4)
	v_pk_fma_f32 v[50:51], v[14:15], v[36:37], v[50:51]
	v_pk_fma_f32 v[52:53], v[12:13], v[34:35], v[52:53]
	buffer_load_dwordx4 v[34:37], v25, s[0:3], s20 offen nt
	v_add_f32_dpp v16, v16, v16 quad_perm:[2,3,0,1] row_mask:0xf bank_mask:0xf bound_ctrl:1
	s_waitcnt vmcnt(4)
	v_pk_fma_f32 v[58:59], v[10:11], v[40:41], v[50:51]
	v_pk_fma_f32 v[38:39], v[8:9], v[38:39], v[52:53]
	v_add_f32_e32 v19, v58, v59
	v_add_f32_e32 v17, v38, v39
	v_add_f32_dpp v58, v60, v60 quad_perm:[1,0,3,2] row_mask:0xf bank_mask:0xf bound_ctrl:1
	v_add_f32_e32 v18, v17, v19
	v_add_f32_dpp v16, v16, v16 row_ror:4 row_mask:0xf bank_mask:0xf bound_ctrl:1
	v_add_f32_dpp v17, v58, v58 quad_perm:[2,3,0,1] row_mask:0xf bank_mask:0xf bound_ctrl:1
	buffer_load_dwordx4 v[20:23], v25, s[0:3], s20 offen offset:2048 nt
	buffer_load_dwordx4 v[46:49], v25, s[0:3], s20 offen offset:3072 nt
	v_add_f32_dpp v17, v17, v17 row_ror:4 row_mask:0xf bank_mask:0xf bound_ctrl:1
	v_add_f32_dpp v58, v16, v16 row_ror:8 row_mask:0xf bank_mask:0xf bound_ctrl:1
	buffer_load_dwordx4 v[38:41], v25, s[0:3], s21 offen nt
	buffer_load_dwordx4 v[50:53], v25, s[0:3], s21 offen offset:1024 nt
	v_add_f32_dpp v17, v17, v17 row_ror:8 row_mask:0xf bank_mask:0xf bound_ctrl:1
	v_mov_b32_e32 v19, v17
	v_mov_b32_e32 v59, v58
	s_nop 0
	v_permlane16_swap_b32_e32 v17, v19
	v_permlane16_swap_b32_e32 v58, v59
	v_add_f32_e32 v16, v17, v19
	v_add_f32_e32 v17, v58, v59
	v_add_f32_dpp v18, v18, v18 quad_perm:[1,0,3,2] row_mask:0xf bank_mask:0xf bound_ctrl:1
	s_waitcnt vmcnt(7)
	v_pk_fma_f32 v[28:29], v[14:15], v[28:29], v[54:55]
	v_pk_fma_f32 v[54:55], v[12:13], v[26:27], v[56:57]
	s_waitcnt vmcnt(6)
	v_pk_fma_f32 v[58:59], v[10:11], v[32:33], v[28:29]
	buffer_load_dwordx4 v[26:29], v25, s[0:3], s21 offen offset:2048 nt
	v_pk_fma_f32 v[54:55], v[8:9], v[30:31], v[54:55]
	buffer_load_dwordx4 v[30:33], v25, s[0:3], s21 offen offset:3072 nt
	v_add_f32_e32 v66, v54, v55
	s_waitcnt vmcnt(7)
	v_pk_mul_f32 v[54:55], v[6:7], v[44:45]
	v_pk_mul_f32 v[56:57], v[4:5], v[42:43]
	buffer_load_dwordx4 v[42:45], v25, s[0:3], s22 offen offset:1024 nt
	s_waitcnt vmcnt(7)
	v_pk_fma_f32 v[54:55], v[2:3], v[36:37], v[54:55]
	v_pk_fma_f32 v[56:57], v[0:1], v[34:35], v[56:57]
	buffer_load_dwordx4 v[34:37], v25, s[0:3], s22 offen nt
	v_add_f32_dpp v18, v18, v18 quad_perm:[2,3,0,1] row_mask:0xf bank_mask:0xf bound_ctrl:1
	s_waitcnt vmcnt(7)
	v_pk_fma_f32 v[22:23], v[14:15], v[22:23], v[54:55]
	v_pk_fma_f32 v[20:21], v[12:13], v[20:21], v[56:57]
	s_waitcnt vmcnt(6)
	v_pk_fma_f32 v[60:61], v[10:11], v[48:49], v[22:23]
	v_pk_fma_f32 v[22:23], v[8:9], v[46:47], v[20:21]
	s_waitcnt vmcnt(4)
	v_pk_mul_f32 v[54:55], v[4:5], v[50:51]
	v_pk_mul_f32 v[20:21], v[6:7], v[52:53]
	v_pk_fma_f32 v[38:39], v[0:1], v[38:39], v[54:55]
	buffer_load_dwordx4 v[46:49], v25, s[0:3], s22 offen offset:2048 nt
	buffer_load_dwordx4 v[50:53], v25, s[0:3], s22 offen offset:3072 nt
	v_pk_fma_f32 v[20:21], v[2:3], v[40:41], v[20:21]
	v_add_f32_e32 v23, v22, v23
	v_add_f32_dpp v18, v18, v18 row_ror:4 row_mask:0xf bank_mask:0xf bound_ctrl:1
	s_waitcnt vmcnt(5)
	v_pk_fma_f32 v[26:27], v[12:13], v[26:27], v[38:39]
	buffer_load_dwordx4 v[38:41], v25, s[0:3], s23 offen nt
	buffer_load_dwordx4 v[54:57], v25, s[0:3], s23 offen offset:1024 nt
	v_pk_fma_f32 v[20:21], v[14:15], v[28:29], v[20:21]
	s_waitcnt vmcnt(6)
	v_pk_fma_f32 v[30:31], v[8:9], v[30:31], v[26:27]
	v_pk_fma_f32 v[62:63], v[10:11], v[32:33], v[20:21]
	v_add_f32_dpp v18, v18, v18 row_ror:8 row_mask:0xf bank_mask:0xf bound_ctrl:1
	s_waitcnt vmcnt(5)
	v_pk_mul_f32 v[20:21], v[6:7], v[44:45]
	v_pk_mul_f32 v[26:27], v[4:5], v[42:43]
	buffer_load_dwordx4 v[42:45], v25, s[0:3], s23 offen offset:2048 nt
	s_waitcnt vmcnt(5)
	v_pk_fma_f32 v[64:65], v[0:1], v[34:35], v[26:27]
	buffer_load_dwordx4 v[32:35], v25, s[0:3], s23 offen offset:3072 nt
	v_add_f32_e32 v27, v60, v61
	v_add_f32_e32 v23, v23, v27
	v_pk_fma_f32 v[36:37], v[2:3], v[36:37], v[20:21]
	v_add_f32_e32 v20, v58, v59
	v_add_f32_dpp v23, v23, v23 quad_perm:[1,0,3,2] row_mask:0xf bank_mask:0xf bound_ctrl:1
	v_add_f32_e32 v20, v66, v20
	v_mov_b32_e32 v19, v18
	v_add_f32_dpp v23, v23, v23 quad_perm:[2,3,0,1] row_mask:0xf bank_mask:0xf bound_ctrl:1
	v_add_f32_dpp v20, v20, v20 quad_perm:[1,0,3,2] row_mask:0xf bank_mask:0xf bound_ctrl:1
	v_permlane16_swap_b32_e32 v18, v19
	v_add_f32_dpp v23, v23, v23 row_ror:4 row_mask:0xf bank_mask:0xf bound_ctrl:1
	v_add_f32_dpp v20, v20, v20 quad_perm:[2,3,0,1] row_mask:0xf bank_mask:0xf bound_ctrl:1
	v_add_f32_e32 v18, v18, v19
	v_add_f32_dpp v23, v23, v23 row_ror:8 row_mask:0xf bank_mask:0xf bound_ctrl:1
	v_mov_b32_e32 v27, v23
	s_nop 1
	v_permlane16_swap_b32_e32 v23, v27
	v_add_f32_e32 v28, v23, v27
	v_add_f32_e32 v23, v30, v31
	s_waitcnt vmcnt(5)
	v_pk_fma_f32 v[30:31], v[14:15], v[48:49], v[36:37]
	v_pk_fma_f32 v[36:37], v[12:13], v[46:47], v[64:65]
	s_waitcnt vmcnt(4)
	v_pk_fma_f32 v[30:31], v[10:11], v[52:53], v[30:31]
	v_pk_fma_f32 v[36:37], v[8:9], v[50:51], v[36:37]
	v_add_f32_e32 v27, v62, v63
	v_add_f32_e32 v36, v36, v37
	v_add_f32_e32 v30, v30, v31
	v_add_f32_e32 v23, v23, v27
	v_add_f32_e32 v30, v36, v30
	v_add_f32_dpp v20, v20, v20 row_ror:4 row_mask:0xf bank_mask:0xf bound_ctrl:1
	v_add_f32_dpp v23, v23, v23 quad_perm:[1,0,3,2] row_mask:0xf bank_mask:0xf bound_ctrl:1
	v_add_f32_dpp v30, v30, v30 quad_perm:[1,0,3,2] row_mask:0xf bank_mask:0xf bound_ctrl:1
	v_add_f32_dpp v20, v20, v20 row_ror:8 row_mask:0xf bank_mask:0xf bound_ctrl:1
	v_add_f32_dpp v23, v23, v23 quad_perm:[2,3,0,1] row_mask:0xf bank_mask:0xf bound_ctrl:1
	v_add_f32_dpp v30, v30, v30 quad_perm:[2,3,0,1] row_mask:0xf bank_mask:0xf bound_ctrl:1
	v_mov_b32_e32 v21, v20
	v_add_f32_dpp v23, v23, v23 row_ror:4 row_mask:0xf bank_mask:0xf bound_ctrl:1
	v_add_f32_dpp v30, v30, v30 row_ror:4 row_mask:0xf bank_mask:0xf bound_ctrl:1
	v_permlane16_swap_b32_e32 v20, v21
	v_add_f32_dpp v23, v23, v23 row_ror:8 row_mask:0xf bank_mask:0xf bound_ctrl:1
	v_add_f32_dpp v30, v30, v30 row_ror:8 row_mask:0xf bank_mask:0xf bound_ctrl:1
	v_mov_b32_e32 v27, v23
	v_mov_b32_e32 v31, v30
	s_nop 0
	v_permlane16_swap_b32_e32 v23, v27
	v_permlane16_swap_b32_e32 v30, v31
	v_add_f32_e32 v21, v20, v21
	v_add_f32_e32 v23, v23, v27
	v_add_f32_e32 v30, v30, v31
	v_mov_b32_e32 v19, v16
	v_mov_b32_e32 v20, v17
	v_mov_b32_e32 v22, v18
	v_mov_b32_e32 v26, v21
	v_mov_b32_e32 v29, v28
	v_mov_b32_e32 v27, v23
	v_mov_b32_e32 v31, v30
	v_permlane32_swap_b32_e32 v16, v19
	v_permlane32_swap_b32_e32 v17, v20
	v_permlane32_swap_b32_e32 v18, v22
	v_permlane32_swap_b32_e32 v21, v26
	v_permlane32_swap_b32_e32 v28, v29
	v_permlane32_swap_b32_e32 v23, v27
	s_waitcnt vmcnt(2)
	v_pk_mul_f32 v[6:7], v[6:7], v[56:57]
	v_pk_mul_f32 v[4:5], v[4:5], v[54:55]
	v_pk_fma_f32 v[2:3], v[2:3], v[40:41], v[6:7]
	v_pk_fma_f32 v[0:1], v[0:1], v[38:39], v[4:5]
	v_permlane32_swap_b32_e32 v30, v31
	s_waitcnt vmcnt(1)
	v_pk_fma_f32 v[2:3], v[14:15], v[44:45], v[2:3]
	v_pk_fma_f32 v[0:1], v[12:13], v[42:43], v[0:1]
	s_waitcnt vmcnt(0)
	v_pk_fma_f32 v[2:3], v[10:11], v[34:35], v[2:3]
	v_pk_fma_f32 v[0:1], v[8:9], v[32:33], v[0:1]
	s_nop 0
	v_add_f32_e32 v0, v0, v1
	v_add_f32_e32 v1, v2, v3
	v_add_f32_e32 v0, v0, v1
	s_nop 1
	v_add_f32_dpp v0, v0, v0 quad_perm:[1,0,3,2] row_mask:0xf bank_mask:0xf bound_ctrl:1
	s_nop 1
	v_add_f32_dpp v0, v0, v0 quad_perm:[2,3,0,1] row_mask:0xf bank_mask:0xf bound_ctrl:1
	s_nop 1
	v_add_f32_dpp v0, v0, v0 row_ror:4 row_mask:0xf bank_mask:0xf bound_ctrl:1
	s_nop 1
	v_add_f32_dpp v0, v0, v0 row_ror:8 row_mask:0xf bank_mask:0xf bound_ctrl:1
	v_mov_b32_e32 v1, v0
	s_nop 1
	v_permlane16_swap_b32_e32 v0, v1
	v_add_f32_e32 v0, v0, v1
	v_mov_b32_e32 v1, v0
	s_nop 1
	v_permlane32_swap_b32_e32 v0, v1
	s_and_saveexec_b64 s[0:1], vcc
	s_cbranch_execz .LBB1_4
	v_add_f32_e32 v6, v16, v19
	v_cmp_eq_u32_e32 vcc, 0, v24
	v_add_f32_e32 v5, v17, v20
	v_add_f32_e32 v4, v18, v22
	v_cndmask_b32_e32 v6, 0, v6, vcc
	v_cmp_eq_u32_e32 vcc, 1, v24
	v_add_f32_e32 v3, v21, v26
	v_add_f32_e32 v2, v28, v29
	v_cndmask_b32_e32 v5, v6, v5, vcc
	v_cmp_eq_u32_e32 vcc, 2, v24
	v_add_f32_e32 v0, v0, v1
	v_add_f32_e32 v1, v30, v31
	v_cndmask_b32_e32 v4, v5, v4, vcc
	v_cmp_eq_u32_e32 vcc, 3, v24
	s_lshl_b32 s0, s8, 13
	s_and_b32 s0, s0, 0x1e000
	v_cndmask_b32_e32 v3, v4, v3, vcc
	v_cmp_eq_u32_e32 vcc, 4, v24
	s_add_u32 s0, s6, s0
	s_addc_u32 s1, s7, 0
	v_cndmask_b32_e32 v2, v3, v2, vcc
	v_add_f32_e32 v3, v23, v27
	v_cmp_eq_u32_e32 vcc, 5, v24
	s_nop 1
	v_cndmask_b32_e32 v2, v2, v3, vcc
	v_cmp_eq_u32_e32 vcc, 6, v24
	s_nop 1
	v_cndmask_b32_e32 v1, v2, v1, vcc
	v_cmp_eq_u32_e32 vcc, 7, v24
	s_nop 1
	v_cndmask_b32_e32 v2, v1, v0, vcc
	v_add_u32_e32 v0, s11, v24
	v_and_b32_e32 v0, 7, v0
	s_lshr_b32 s9, s9, 4
	v_add_u32_e32 v0, s9, v0
	v_ashrrev_i32_e32 v1, 31, v0
	v_lshl_add_u64 v[0:1], v[0:1], 2, s[0:1]
	v_add_co_u32_e32 v0, vcc, 0x6000, v0
	s_nop 1
	v_addc_co_u32_e32 v1, vcc, 0, v1, vcc
	global_store_dword v[0:1], v2, off offset:64

amdhsa.kernels:
  - .agpr_count:     0
    .args:
      - .actual_access:  read_only
        .address_space:  global
        .offset:         0
        .size:           8
        .value_kind:     global_buffer
      - .actual_access:  read_only
        .address_space:  global
        .offset:         8
        .size:           8
        .value_kind:     global_buffer
      - .actual_access:  read_only
        .address_space:  global
        .offset:         16
        .size:           8
        .value_kind:     global_buffer
      - .actual_access:  read_only
        .address_space:  global
        .offset:         24
        .size:           8
        .value_kind:     global_buffer
      - .actual_access:  write_only
        .address_space:  global
        .offset:         32
        .size:           8
        .value_kind:     global_buffer
    .group_segment_fixed_size: 2112
    .kernarg_segment_align: 8
    .kernarg_segment_size: 40
    .language:       OpenCL C
    .language_version:
      - 2
      - 0
    .max_flat_workgroup_size: 1024
    .name:           _Z11prep_kernelPKfS0_S0_S0_Pf
    .private_segment_fixed_size: 0
    .sgpr_count:     34
    .sgpr_spill_count: 0
    .symbol:         _Z11prep_kernelPKfS0_S0_S0_Pf.kd
    .uniform_work_group_size: 1
    .uses_dynamic_stack: false
    .vgpr_count:     72
    .vgpr_spill_count: 0
    .wavefront_size: 64
  - .agpr_count:     0
    .args:
      - .actual_access:  read_only
        .address_space:  global
        .offset:         0
        .size:           8
        .value_kind:     global_buffer
      - .address_space:  global
        .offset:         8
        .size:           8
        .value_kind:     global_buffer
    .group_segment_fixed_size: 4096
    .kernarg_segment_align: 8
    .kernarg_segment_size: 16
    .language:       OpenCL C
    .language_version:
      - 2
      - 0
    .max_flat_workgroup_size: 1024
    .name:           _Z13stream_kernelPKfPf
    .private_segment_fixed_size: 0
    .sgpr_count:     30
    .sgpr_spill_count: 0
    .symbol:         _Z13stream_kernelPKfPf.kd
    .uniform_work_group_size: 1
    .uses_dynamic_stack: false
    .vgpr_count:     67
    .vgpr_spill_count: 0
    .wavefront_size: 64
  - .agpr_count:     0
    .args:
      - .actual_access:  read_only
        .address_space:  global
        .offset:         0
        .size:           8
        .value_kind:     global_buffer
      - .actual_access:  write_only
        .address_space:  global
        .offset:         8
        .size:           8
        .value_kind:     global_buffer
    .group_segment_fixed_size: 32
    .kernarg_segment_align: 8
    .kernarg_segment_size: 16
    .language:       OpenCL C
    .language_version:
      - 2
      - 0
    .max_flat_workgroup_size: 256
    .name:           _Z14softmax_kernelPKfPf
    .private_segment_fixed_size: 0
    .sgpr_count:     26
    .sgpr_spill_count: 0
    .symbol:         _Z14softmax_kernelPKfPf.kd
    .uniform_work_group_size: 1
    .uses_dynamic_stack: false
    .vgpr_count:     32
    .vgpr_spill_count: 0
    .wavefront_size: 64
